# speedup vs baseline: 1.0078x; 1.0008x over previous
.LBB0_47:
	s_or_b64 exec, exec, s[0:1]
	s_waitcnt vmcnt(32)
	v_mul_f32_e32 v0, 0x3fb8aa3b, v28
	v_mul_f32_e32 v1, 0x3fb8aa3b, v29
	v_mul_f32_e32 v2, 0x3fb8aa3b, v30
	v_mul_f32_e32 v3, 0x3fb8aa3b, v31
	v_mul_f32_e32 v4, 0x3fb8aa3b, v24
	v_mul_f32_e32 v5, 0x3fb8aa3b, v25
	v_mul_f32_e32 v6, 0x3fb8aa3b, v26
	v_mul_f32_e32 v7, 0x3fb8aa3b, v27
	v_exp_f32_e32 v0, v0
	v_exp_f32_e32 v1, v1
	v_exp_f32_e32 v2, v2
	v_exp_f32_e32 v3, v3
	v_exp_f32_e32 v4, v4
	v_exp_f32_e32 v5, v5
	v_exp_f32_e32 v6, v6
	v_exp_f32_e32 v7, v7
	v_add_f32_e32 v0, -1.0, v0
	v_add_f32_e32 v1, -1.0, v1
	v_add_f32_e32 v2, -1.0, v2
	v_add_f32_e32 v3, -1.0, v3
	v_add_f32_e32 v4, -1.0, v4
	v_add_f32_e32 v5, -1.0, v5
	v_add_f32_e32 v6, -1.0, v6
	v_add_f32_e32 v7, -1.0, v7
	v_cmp_lt_f32_e64 s[0:1], 0, v28
	v_cmp_lt_f32_e64 s[2:3], 0, v29
	v_cmp_lt_f32_e64 s[4:5], 0, v30
	v_cmp_lt_f32_e64 s[6:7], 0, v31
	v_cndmask_b32_e64 v8, v0, v28, s[0:1]
	v_cndmask_b32_e64 v9, v1, v29, s[2:3]
	v_cndmask_b32_e64 v10, v2, v30, s[4:5]
	v_cndmask_b32_e64 v11, v3, v31, s[6:7]
	v_cmp_lt_f32_e64 s[0:1], 0, v24
	v_cmp_lt_f32_e64 s[2:3], 0, v25
	v_cmp_lt_f32_e64 s[4:5], 0, v26
	v_cmp_lt_f32_e64 s[6:7], 0, v27
	v_cndmask_b32_e64 v12, v4, v24, s[0:1]
	v_cndmask_b32_e64 v13, v5, v25, s[2:3]
	v_cndmask_b32_e64 v14, v6, v26, s[4:5]
	v_cndmask_b32_e64 v15, v7, v27, s[6:7]
	v_mul_f32_e32 v0, 0x3fb8aa3b, v8
	v_mul_f32_e32 v1, 0x3fb8aa3b, v9
	v_mul_f32_e32 v2, 0x3fb8aa3b, v10
	v_mul_f32_e32 v3, 0x3fb8aa3b, v11
	v_mul_f32_e32 v4, 0x3fb8aa3b, v12
	v_mul_f32_e32 v5, 0x3fb8aa3b, v13
	v_mul_f32_e32 v6, 0x3fb8aa3b, v14
	v_mul_f32_e32 v7, 0x3fb8aa3b, v15
	v_exp_f32_e32 v0, v0
	v_exp_f32_e32 v1, v1
	v_exp_f32_e32 v2, v2
	v_exp_f32_e32 v3, v3
	v_exp_f32_e32 v4, v4
	v_exp_f32_e32 v5, v5
	v_exp_f32_e32 v6, v6
	v_exp_f32_e32 v7, v7
	v_add_f32_e32 v0, -1.0, v0
	v_add_f32_e32 v1, -1.0, v1
	v_add_f32_e32 v2, -1.0, v2
	v_add_f32_e32 v3, -1.0, v3
	v_add_f32_e32 v4, -1.0, v4
	v_add_f32_e32 v5, -1.0, v5
	v_add_f32_e32 v6, -1.0, v6
	v_add_f32_e32 v7, -1.0, v7
	v_cmp_lt_f32_e64 s[0:1], 0, v8
	v_cmp_lt_f32_e64 s[2:3], 0, v9
	v_cmp_lt_f32_e64 s[4:5], 0, v10
	v_cmp_lt_f32_e64 s[6:7], 0, v11
	v_cndmask_b32_e64 v16, v0, v8, s[0:1]
	v_cndmask_b32_e64 v17, v1, v9, s[2:3]
	v_cndmask_b32_e64 v18, v2, v10, s[4:5]
	v_cndmask_b32_e64 v19, v3, v11, s[6:7]
	v_cmp_lt_f32_e64 s[0:1], 0, v12
	v_cmp_lt_f32_e64 s[2:3], 0, v13
	v_cmp_lt_f32_e64 s[4:5], 0, v14
	v_cmp_lt_f32_e64 s[6:7], 0, v15
	v_cndmask_b32_e64 v20, v4, v12, s[0:1]
	v_cndmask_b32_e64 v21, v5, v13, s[2:3]
	v_cndmask_b32_e64 v22, v6, v14, s[4:5]
	v_cndmask_b32_e64 v23, v7, v15, s[6:7]
	v_cvt_pk_f16_f32 v0, v16, v17
	v_cvt_pk_f16_f32 v1, v18, v19
	v_cvt_pk_f16_f32 v2, v20, v21
	v_cvt_pk_f16_f32 v3, v22, v23
	ds_write_b128 v95, v[0:3]
	s_waitcnt lgkmcnt(0)
	s_barrier
	ds_read_b128 v[0:3], v94
	ds_read_b128 v[4:7], v94 offset:1024
	ds_read_b128 v[8:11], v94 offset:2048
	ds_read_b128 v[12:15], v94 offset:3072
	s_cbranch_vccz .Lprep_v
	s_waitcnt vmcnt(16)
	s_branch .Lprep_w
.Lprep_v:
	s_waitcnt vmcnt(0)
.Lprep_w:
	v_cvt_pk_f16_f32 v16, v77, v78
	v_cvt_pk_f16_f32 v17, v79, v80
	v_cvt_pk_f16_f32 v18, v81, v82
	v_cvt_pk_f16_f32 v19, v83, v84
	v_cvt_pk_f16_f32 v20, v69, v70
	v_cvt_pk_f16_f32 v21, v71, v72
	v_cvt_pk_f16_f32 v22, v73, v74
	v_cvt_pk_f16_f32 v23, v75, v76
	v_cvt_pk_f16_f32 v24, v61, v62
	v_cvt_pk_f16_f32 v25, v63, v64
	v_cvt_pk_f16_f32 v26, v65, v66
	v_cvt_pk_f16_f32 v27, v67, v68
	v_cvt_pk_f16_f32 v28, v32, v35
	v_cvt_pk_f16_f32 v29, v40, v41
	v_cvt_pk_f16_f32 v30, v42, v43
	v_cvt_pk_f16_f32 v31, v47, v48
	s_waitcnt lgkmcnt(0)
	v_mfma_f32_32x32x16_f16 a[0:15], v[16:19], v[0:3], 0
	v_mfma_f32_32x32x16_f16 a[0:15], v[20:23], v[4:7], a[0:15]
	v_mfma_f32_32x32x16_f16 a[0:15], v[24:27], v[8:11], a[0:15]
	v_mfma_f32_32x32x16_f16 a[0:15], v[28:31], v[12:15], a[0:15]
	v_lshlrev_b32_e32 v0, 3, v39
	v_or3_b32 v6, v0, v34, v38
	v_lshl_add_u64 v[4:5], s[8:9], 0, v[36:37]
	s_waitcnt vmcnt(0)
	s_nop 9
	v_accvgpr_read_b32 v0, a0
	v_add_f32_e32 v0, v0, v44
	v_add_f32_e32 v1, 1.0, v0
	v_cndmask_b32_e32 v2, v0, v1, vcc
	v_mul_f32_e32 v0, 0x3fb8aa3b, v0
	v_exp_f32_e32 v7, v0
	v_accvgpr_read_b32 v0, a1
	v_add_f32_e32 v0, v0, v33
	v_add_f32_e32 v1, 1.0, v0
	v_cndmask_b32_e32 v3, v0, v1, vcc
	v_mul_f32_e32 v0, 0x3fb8aa3b, v0
	v_exp_f32_e32 v8, v0
	v_accvgpr_read_b32 v0, a2
	v_add_f32_e32 v0, v0, v50
	v_add_f32_e32 v1, 1.0, v0
	v_cndmask_b32_e32 v1, v0, v1, vcc
	v_mul_f32_e32 v0, 0x3fb8aa3b, v0
	v_exp_f32_e32 v9, v0
	v_accvgpr_read_b32 v0, a3
	v_add_f32_e32 v0, v0, v46
	v_mul_f32_e32 v11, 0x3fb8aa3b, v0
	v_exp_f32_e32 v11, v11
	v_add_f32_e32 v10, 1.0, v0
	v_cndmask_b32_e32 v0, v0, v10, vcc
	v_cvt_pk_f16_f32 v1, v1, v0
	v_cvt_pk_f16_f32 v0, v2, v3
	v_cvt_pk_f16_f32 v2, v7, v8
	v_ashrrev_i32_e32 v7, 31, v6
	v_cvt_pk_f16_f32 v3, v9, v11
	v_lshl_add_u64 v[4:5], v[6:7], 4, v[4:5]
	global_store_dwordx4 v[4:5], v[0:3], off
	s_nop 1
	v_accvgpr_read_b32 v0, a4
	v_add_f32_e32 v0, v0, v49
	v_add_f32_e32 v1, 1.0, v0
	v_cndmask_b32_e32 v2, v0, v1, vcc
	v_mul_f32_e32 v0, 0x3fb8aa3b, v0
	v_exp_f32_e32 v6, v0
	v_accvgpr_read_b32 v0, a5
	v_add_f32_e32 v0, v0, v45
	v_add_f32_e32 v1, 1.0, v0
	v_cndmask_b32_e32 v3, v0, v1, vcc
	v_mul_f32_e32 v0, 0x3fb8aa3b, v0
	v_exp_f32_e32 v7, v0
	v_accvgpr_read_b32 v0, a6
	v_add_f32_e32 v0, v0, v53
	v_add_f32_e32 v1, 1.0, v0
	v_cndmask_b32_e32 v1, v0, v1, vcc
	v_mul_f32_e32 v0, 0x3fb8aa3b, v0
	v_exp_f32_e32 v8, v0
	v_accvgpr_read_b32 v0, a7
	v_add_f32_e32 v0, v0, v51
	v_mul_f32_e32 v10, 0x3fb8aa3b, v0
	v_exp_f32_e32 v10, v10
	v_add_f32_e32 v9, 1.0, v0
	v_cndmask_b32_e32 v0, v0, v9, vcc
	v_cvt_pk_f16_f32 v1, v1, v0
	v_cvt_pk_f16_f32 v0, v2, v3
	v_cvt_pk_f16_f32 v3, v8, v10
	v_cvt_pk_f16_f32 v2, v6, v7
	global_store_dwordx4 v[4:5], v[0:3], off offset:32
	s_nop 1
	v_accvgpr_read_b32 v0, a8
	v_add_f32_e32 v0, v0, v54
	v_add_f32_e32 v1, 1.0, v0
	v_cndmask_b32_e32 v2, v0, v1, vcc
	v_mul_f32_e32 v0, 0x3fb8aa3b, v0
	v_exp_f32_e32 v6, v0
	v_accvgpr_read_b32 v0, a9
	v_add_f32_e32 v0, v0, v52
	v_add_f32_e32 v1, 1.0, v0
	v_cndmask_b32_e32 v3, v0, v1, vcc
	v_mul_f32_e32 v0, 0x3fb8aa3b, v0
	v_exp_f32_e32 v7, v0
	v_accvgpr_read_b32 v0, a10
	v_add_f32_e32 v0, v0, v57
	v_add_f32_e32 v1, 1.0, v0
	v_cndmask_b32_e32 v1, v0, v1, vcc
	v_mul_f32_e32 v0, 0x3fb8aa3b, v0
	v_exp_f32_e32 v8, v0
	v_accvgpr_read_b32 v0, a11
	v_add_f32_e32 v0, v0, v55
	v_mul_f32_e32 v10, 0x3fb8aa3b, v0
	v_exp_f32_e32 v10, v10
	v_add_f32_e32 v9, 1.0, v0
	v_cndmask_b32_e32 v0, v0, v9, vcc
	v_cvt_pk_f16_f32 v1, v1, v0
	v_cvt_pk_f16_f32 v0, v2, v3
	v_cvt_pk_f16_f32 v3, v8, v10
	v_cvt_pk_f16_f32 v2, v6, v7
	global_store_dwordx4 v[4:5], v[0:3], off offset:64
	s_nop 1
	v_accvgpr_read_b32 v0, a12
	v_add_f32_e32 v0, v0, v58
	v_add_f32_e32 v1, 1.0, v0
	v_cndmask_b32_e32 v2, v0, v1, vcc
	v_mul_f32_e32 v0, 0x3fb8aa3b, v0
	v_exp_f32_e32 v6, v0
	v_accvgpr_read_b32 v0, a13
	v_add_f32_e32 v0, v0, v56
	v_add_f32_e32 v1, 1.0, v0
	v_cndmask_b32_e32 v3, v0, v1, vcc
	v_mul_f32_e32 v0, 0x3fb8aa3b, v0
	v_exp_f32_e32 v7, v0
	v_accvgpr_read_b32 v0, a14
	v_add_f32_e32 v0, v0, v60
	v_add_f32_e32 v1, 1.0, v0
	v_cndmask_b32_e32 v1, v0, v1, vcc
	v_mul_f32_e32 v0, 0x3fb8aa3b, v0
	v_exp_f32_e32 v8, v0
	v_accvgpr_read_b32 v0, a15
	v_add_f32_e32 v0, v0, v59
	v_mul_f32_e32 v10, 0x3fb8aa3b, v0
	v_exp_f32_e32 v10, v10
	v_add_f32_e32 v9, 1.0, v0
	v_cndmask_b32_e32 v0, v0, v9, vcc
	v_cvt_pk_f16_f32 v1, v1, v0
	v_cvt_pk_f16_f32 v0, v2, v3
	v_cvt_pk_f16_f32 v3, v8, v10
	v_cvt_pk_f16_f32 v2, v6, v7
	global_store_dwordx4 v[4:5], v[0:3], off offset:96
	s_endpgm

.LBB1_235:
	v_add_u32_e32 v0, s66, v0
	v_subrev_u32_e32 v0, 0x100, v0
	s_movk_i32 s0, 0xf0
	v_cmp_gt_u32_e32 vcc, s0, v0
	s_and_saveexec_b64 s[0:1], vcc
	s_cbranch_execz .Lepi_idle
	s_load_dwordx4 s[68:71], s[14:15], 0x0
	s_load_dwordx2 s[72:73], s[14:15], 0x10
	s_movk_i32 s0, 0x77
	v_mov_b32_e32 v1, 0xffffff88
	v_cmp_lt_u32_e32 vcc, s0, v0
	v_mov_b32_e32 v2, 0x44704000
	s_mov_b32 s0, 0xf800000
	v_cndmask_b32_e32 v1, 0, v1, vcc
	v_add_u32_e32 v0, v1, v0
	v_cvt_f32_u32_e32 v1, v0
	s_mov_b32 s5, 0x17800
	s_mov_b32 s4, 0x3eb17218
	v_fmac_f32_e32 v2, 0xc1000000, v1
	v_sqrt_f32_e32 v1, v2
	s_nop 0
	v_sub_f32_e32 v1, 0x41f80000, v1
	v_mul_f32_e32 v1, 0.5, v1
	v_cvt_i32_f32_e32 v1, v1
	s_and_b64 s[0:1], exec, s[16:17]
	s_cselect_b32 s2, s40, s38
	s_cselect_b32 s3, s39, s33
	v_sub_u32_e32 v2, 31, v1
	v_mul_lo_u32 v2, v2, v1
	v_lshrrev_b32_e32 v3, 31, v2
	v_add_u32_e32 v2, v2, v3
	v_ashrrev_i32_e32 v2, 1, v2
	v_cmp_gt_i32_e64 s[0:1], v2, v0
	s_nop 1
	v_subbrev_co_u32_e64 v1, s[0:1], 0, v1, s[0:1]
	v_add_u32_e32 v2, 1, v1
	v_sub_u32_e32 v3, 30, v1
	v_mul_lo_u32 v3, v2, v3
	v_lshrrev_b32_e32 v4, 31, v3
	v_add_u32_e32 v3, v3, v4
	v_ashrrev_i32_e32 v3, 1, v3
	v_cmp_gt_i32_e64 s[0:1], v3, v0
	s_nop 1
	v_cndmask_b32_e64 v12, v2, v1, s[0:1]
	v_sub_u32_e32 v1, 31, v12
	v_mul_lo_u32 v1, v1, v12
	v_lshrrev_b32_e32 v2, 31, v1
	v_add_u32_e32 v1, v1, v2
	v_ashrrev_i32_e32 v1, 1, v1
	v_sub_u32_e32 v0, v0, v1
	v_cndmask_b32_e64 v1, 0, 16, vcc
	v_lshl_or_b32 v1, s2, 5, v1
	v_add_u32_e32 v1, v1, v12
	v_sub_u32_e32 v2, 0xff, v1
	v_mul_lo_u32 v1, v2, v1
	v_lshrrev_b32_e32 v2, 31, v1
	v_add_u32_e32 v1, v1, v2
	v_ashrrev_i32_e32 v1, 1, v1
	v_add3_u32 v13, v12, v0, 1
	v_add_u32_e32 v0, v1, v0
	v_ashrrev_i32_e32 v1, 31, v0
	v_mov_b32_e32 v2, 0x1fc0
	v_mad_u64_u32 v[0:1], s[0:1], s3, v2, v[0:1]
	v_mad_u64_u32 v[4:5], s[0:1], v0, 24, s[10:11]
	v_mov_b32_e32 v0, 0x17800
	v_lshl_add_u32 v14, v12, 2, v0
	v_mov_b32_e32 v0, 0x60
	v_cndmask_b32_e32 v15, 0, v0, vcc
	v_or_b32_e32 v2, 16, v15
	v_add_lshl_u32 v3, v2, v12, 6
	v_add_u32_e32 v2, v2, v13
	v_lshl_add_u32 v6, v2, 6, v14
	v_add_u32_e32 v2, 32, v15
	v_add_lshl_u32 v7, v2, v12, 6
	v_add_u32_e32 v2, v2, v13
	v_lshl_add_u32 v8, v2, 6, v14
	v_add_u32_e32 v2, 48, v15
	v_mad_i32_i24 v5, v1, 24, v5
	v_add_lshl_u32 v0, v15, v12, 6
	v_lshlrev_b32_e32 v16, 2, v13
	v_add_u32_e32 v1, v15, v13
	v_add_lshl_u32 v9, v2, v12, 6
	v_add_u32_e32 v17, 64, v15
	v_add_u32_e32 v15, 0x50, v15
	v_add3_u32 v0, v0, v16, s5
	v_lshl_add_u32 v1, v1, 6, v14
	v_add3_u32 v3, v3, v16, s5
	v_add3_u32 v7, v7, v16, s5
	v_add3_u32 v9, v9, v16, s5
	v_add_u32_e32 v2, v2, v13
	v_add_lshl_u32 v18, v17, v12, 6
	v_add_lshl_u32 v12, v15, v12, 6
	v_lshl_add_u32 v10, v2, 6, v14
	ds_read_b32 v0, v0
	ds_read_b32 v2, v1
	ds_read_b32 v1, v3
	ds_read_b32 v3, v6
	ds_read_b32 v6, v7
	ds_read_b32 v8, v8
	ds_read_b32 v7, v9
	ds_read_b32 v9, v10
	v_add3_u32 v18, v18, v16, s5
	v_add3_u32 v16, v12, v16, s5
	v_add_u32_e32 v12, v15, v13
	v_add_u32_e32 v17, v17, v13
	v_lshl_add_u32 v15, v12, 6, v14
	v_lshl_add_u32 v17, v17, 6, v14
	ds_read_b32 v12, v18
	ds_read_b32 v14, v17
	ds_read_b32 v13, v16
	ds_read_b32 v15, v15
	s_waitcnt lgkmcnt(0)
	v_pk_add_f32 v[0:1], v[0:1], v[2:3]
	v_mov_b32_e32 v2, s70
	v_mov_b32_e32 v3, s71
	v_mov_b64_e32 v[10:11], s[68:69]
	v_pk_add_f32 v[6:7], v[6:7], v[8:9]
	v_pk_fma_f32 v[0:1], v[0:1], s[4:5], v[10:11] op_sel_hi:[1,0,1]
	v_pk_fma_f32 v[2:3], v[6:7], s[4:5], v[2:3] op_sel_hi:[1,0,1]
	global_store_dwordx4 v[4:5], v[0:3], off
	s_nop 1
	v_pk_add_f32 v[0:1], v[12:13], v[14:15]
	v_mov_b64_e32 v[2:3], s[72:73]
	v_pk_fma_f32 v[0:1], v[0:1], s[4:5], v[2:3] op_sel_hi:[1,0,1]
	global_store_dwordx2 v[4:5], v[0:1], off offset:16
	s_endpgm
